# baseline (speedup 1.0000x reference)
_Z8knn_gemmPKcS0_Pi:
	s_ashr_i32 s3, s2, 31
	s_lshr_b32 s3, s3, 29
	s_add_i32 s3, s2, s3
	s_ashr_i32 s4, s3, 3
	s_and_b32 s3, s3, -8
	s_sub_i32 s3, s2, s3
	s_cmp_lt_i32 s3, 0
	s_movk_i32 s12, 0x188
	s_cselect_b32 s5, s12, 0x187
	s_mul_i32 s3, s5, s3
	s_add_i32 s3, s3, s4
	s_ashr_i32 s4, s3, 31
	s_lshr_b32 s4, s4, 27
	s_add_i32 s10, s3, s4
	s_ashr_i32 s4, s10, 5
	s_lshl_b32 s11, s4, 2
	s_sub_i32 s4, 0x187, s11
	s_min_i32 s13, s4, 4
	s_abs_i32 s14, s13
	v_cvt_f32_u32_e32 v1, s14
	s_andn2_b32 s10, s10, 31
	s_load_dwordx4 s[4:7], s[0:1], 0x0
	s_load_dwordx2 s[8:9], s[0:1], 0x10
	s_sub_i32 s0, s3, s10
	v_rcp_iflag_f32_e32 v1, v1
	s_sub_i32 s10, 0, s14
	s_abs_i32 s3, s0
	s_xor_b32 s1, s0, s13
	v_mul_f32_e32 v1, 0x4f7ffffe, v1
	v_cvt_u32_f32_e32 v1, v1
	s_ashr_i32 s1, s1, 31
	v_lshrrev_b32_e32 v2, 8, v0
	v_lshlrev_b32_e32 v168, 4, v0
	v_readfirstlane_b32 s15, v1
	s_mul_i32 s10, s10, s15
	s_mul_hi_u32 s10, s15, s10
	s_add_i32 s15, s15, s10
	s_mul_hi_u32 s10, s3, s15
	s_mul_i32 s15, s10, s14
	s_sub_i32 s3, s3, s15
	s_add_i32 s15, s10, 1
	s_sub_i32 s16, s3, s14
	s_cmp_ge_u32 s3, s14
	s_cselect_b32 s10, s15, s10
	s_cselect_b32 s3, s16, s3
	s_add_i32 s15, s10, 1
	s_cmp_ge_u32 s3, s14
	s_cselect_b32 s3, s15, s10
	s_xor_b32 s3, s3, s1
	s_sub_i32 s34, s3, s1
	s_mul_i32 s1, s34, s13
	s_sub_i32 s0, s0, s1
	s_add_i32 s11, s11, s0
	v_readfirstlane_b32 s1, v0
	s_sub_i32 s13, 0x186, s11
	s_lshl_b32 s3, s1, 4
	s_mul_i32 s10, s34, 0x30000
	s_mul_hi_i32 s1, s34, 0x30000
	s_waitcnt lgkmcnt(0)
	s_add_u32 s10, s6, s10
	s_addc_u32 s11, s7, s1
	s_mul_i32 s14, s13, 0x30000
	s_mul_hi_i32 s1, s13, 0x30000
	s_add_u32 s22, s4, s14
	v_readfirstlane_b32 s0, v2
	s_addc_u32 s23, s5, s1
	s_cmp_eq_u32 s0, 0
	s_cselect_b64 s[0:1], -1, 0
	s_add_u32 s16, s10, 0x2000
	s_addc_u32 s17, s11, 0
	s_add_u32 s18, s22, 0xfffff000
	s_addc_u32 s19, s23, -1
	s_and_b64 s[14:15], s[0:1], exec
	s_cselect_b32 s17, s17, s19
	s_cselect_b32 s16, s16, s18
	s_add_u32 s18, s22, 0x1000
	s_addc_u32 s19, s23, 0
	s_add_i32 s14, s3, 0
	s_mov_b64 s[20:21], s[10:11]
	s_add_i32 s15, s14, 0x2000
	v_lshrrev_b32_e32 v5, 2, v0
	v_lshrrev_b32_e32 v1, 4, v0
	s_add_i32 s16, s14, 0x4000
	v_and_b32_e32 v5, 2, v5
	s_add_u32 s18, s10, 0x3000
	s_addc_u32 s19, s11, 0
	s_add_u32 s3, s10, 0x5000
	s_addc_u32 s17, s11, 0
	s_add_u32 s20, s22, 0x2000
	s_addc_u32 s21, s23, 0
	s_and_b64 s[10:11], s[0:1], exec
	s_cselect_b32 s11, s17, s21
	s_cselect_b32 s10, s3, s20
	s_add_u32 s20, s22, 0x4000
	s_addc_u32 s21, s23, 0
	s_add_i32 s17, s14, 0x6000
	v_add_lshl_u32 v1, v5, v1, 3
	s_add_i32 s18, s14, 0x8000
	s_add_i32 s19, s14, 0xa000
	v_and_b32_e32 v3, 15, v0
	v_and_b32_e32 v5, 24, v1
	v_lshrrev_b32_e32 v1, 1, v0
	s_movk_i32 s3, 0x60
	s_add_i32 s20, s14, 0xc000
	v_and_or_b32 v1, v1, s3, v3
	v_lshl_or_b32 v2, v2, 6, v3
	s_add_u32 s21, s4, 0x12000
	v_and_b32_e32 v4, 48, v0
	v_mad_u32_u24 v6, v1, s3, 0
	v_mad_u32_u24 v2, v2, s3, 0
	s_addc_u32 s22, s5, 0
	v_add_u32_e32 v1, v6, v4
	v_add_u32_e32 v170, v2, v4
	v_add_u32_e32 v172, v6, v5
	v_add_u32_e32 v173, v2, v5
	v_mov_b32_e32 v39, 0
	s_add_u32 s23, s6, 0x12000
	v_add_u32_e32 v171, 0x3000, v170
	v_add_u32_e32 v174, 0x3040, v173
	v_mov_b32_e32 v169, v39
	v_add_u32_e32 v175, 0x12000, v1
	v_add_u32_e32 v176, 0x12040, v172
	v_add_u32_e32 v177, 0x15000, v170
	v_add_u32_e32 v178, 0x15040, v173
	v_add_u32_e32 v179, 0x12600, v1
	v_add_u32_e32 v180, 0x12640, v172
	v_add_u32_e32 v181, 0x15600, v170
	v_add_u32_e32 v182, 0x15640, v173
	v_add_u32_e32 v183, 0x15c00, v170
	v_add_u32_e32 v184, 0x15c40, v173
	v_add_u32_e32 v185, 0x16200, v170
	v_add_u32_e32 v186, 0x16240, v173
	s_addc_u32 s24, s7, 0
	v_mov_b32_e32 v187, 0x7f7f7f7f
	s_add_i32 s25, 0, 0x18000
	s_movk_i32 s26, 0xff80
	s_movk_i32 s27, 0x30e
	s_add_i32 s28, s14, 0xe000
	s_add_i32 s29, s20, 0x4000
	s_add_i32 s30, s14, 0x12000
	s_add_i32 s31, s14, 0x14000
	s_add_i32 s33, s14, 0x16000
	s_lshr_b32 s66, s14, 12
	s_and_b32 s54, s14, 0xfff
	s_mul_i32 s67, s66, 0x6000
	s_add_i32 s54, s54, s67
	s_add_i32 s55, s54, 0x1000
	s_add_i32 s56, s54, 0x2000
	s_add_i32 s57, s54, 0x3000
	s_add_i32 s58, s54, 0x4000
	s_add_i32 s59, s54, 0x5000
	s_add_i32 s60, s54, 0xc000
	s_add_i32 s61, s54, 0xd000
	s_add_i32 s62, s54, 0xe000
	s_add_i32 s63, s54, 0xf000
	s_add_i32 s64, s54, 0x10000
	s_add_i32 s65, s54, 0x11000
	v_and_b32_e32 v228, 0xfff, v168
	v_add_u32_e32 v229, 0x1000, v228
	v_add_u32_e32 v230, 0x2000, v228
	s_mul_i32 s68, s34, 0x30000
	s_mul_hi_i32 s69, s34, 0x30000
	s_add_u32 s68, s6, s68
	s_addc_u32 s69, s7, s69
	s_mul_i32 s70, s13, 0x30000
	s_mul_hi_i32 s71, s13, 0x30000
	s_add_u32 s70, s4, s70
	s_addc_u32 s71, s5, s71
	s_mul_i32 s67, s66, 0x3000
	s_add_u32 s68, s68, s67
	s_addc_u32 s69, s69, 0
	s_add_u32 s70, s70, s67
	s_addc_u32 s71, s71, 0
	s_mov_b32 m0, s54
	s_nop 0
	global_load_lds_dwordx4 v228, s[68:69]
	s_mov_b32 m0, s55
	s_nop 0
	global_load_lds_dwordx4 v229, s[68:69]
	s_mov_b32 m0, s56
	s_nop 0
	global_load_lds_dwordx4 v230, s[68:69]
	s_mov_b32 m0, s57
	s_nop 0
	global_load_lds_dwordx4 v228, s[70:71]
	s_mov_b32 m0, s58
	s_nop 0
	global_load_lds_dwordx4 v229, s[70:71]
	s_mov_b32 m0, s59
	s_nop 0
	global_load_lds_dwordx4 v230, s[70:71]
	s_waitcnt vmcnt(0)
	s_barrier
	s_add_u32 s68, s68, 0x6000
	s_addc_u32 s69, s69, 0
	s_add_u32 s70, s70, 0x6000
	s_addc_u32 s71, s71, 0
	s_mov_b32 m0, s60
	s_nop 0
	global_load_lds_dwordx4 v228, s[68:69]
	s_mov_b32 m0, s61
	s_nop 0
	global_load_lds_dwordx4 v229, s[68:69]
	s_mov_b32 m0, s62
	s_nop 0
	global_load_lds_dwordx4 v230, s[68:69]
	s_mov_b32 m0, s63
	s_nop 0
	global_load_lds_dwordx4 v228, s[70:71]
	s_mov_b32 m0, s64
	s_nop 0
	global_load_lds_dwordx4 v229, s[70:71]
	s_mov_b32 m0, s65
	s_nop 0
	global_load_lds_dwordx4 v230, s[70:71]
	ds_read_b128 v[2:5], v170 offset:12288
	ds_read_b64 v[6:7], v173 offset:12352
	ds_read_b128 v[8:11], v170 offset:13824
	ds_read_b64 v[12:13], v173 offset:13888
	ds_read_b128 v[14:17], v170 offset:15360
	ds_read_b64 v[18:19], v173 offset:15424
	ds_read_b128 v[26:29], v170 offset:16896
	ds_read_b64 v[30:31], v173 offset:16960
	ds_read_b128 v[20:23], v1
	ds_read_b64 v[24:25], v172 offset:64
	ds_read_b128 v[32:35], v1 offset:1536
	ds_read_b64 v[36:37], v172 offset:1600
	s_branch .LBB1_2
.LBB1_1:
	v_mov_b32_e32 v215, 0
	v_and_b32_e32 v194, 0xffffff80, v164
	v_and_or_b32 v195, v165, s26, 1
	v_max_i32_e32 v196, v194, v195
	v_min_i32_e32 v197, v194, v195
	v_and_or_b32 v198, v166, s26, 2
	v_max_i32_e32 v196, v196, v198
	v_med3_i32 v194, v194, v195, v198
	v_min_i32_e32 v195, v197, v198
	v_and_or_b32 v197, v167, s26, 3
	v_max_i32_e32 v198, v196, v197
	v_med3_i32 v196, v196, v194, v197
	v_min_i32_e32 v194, v194, v197
	v_max_i32_e32 v194, v195, v194
	v_and_or_b32 v195, v160, s26, 4
	v_max_i32_e32 v197, v198, v195
	v_med3_i32 v198, v198, v196, v195
	v_med3_i32 v194, v196, v194, v195
	v_and_or_b32 v195, v161, s26, 5
	v_max_i32_e32 v196, v197, v195
	v_med3_i32 v197, v197, v198, v195
	v_med3_i32 v194, v198, v194, v195
	v_and_or_b32 v195, v162, s26, 6
	v_max_i32_e32 v198, v196, v195
	v_med3_i32 v196, v196, v197, v195
	v_med3_i32 v194, v197, v194, v195
	v_and_or_b32 v195, v163, s26, 7
	v_max_i32_e32 v197, v198, v195
	v_med3_i32 v198, v198, v196, v195
	v_med3_i32 v194, v196, v194, v195
	v_and_or_b32 v195, v156, s26, 8
	v_max_i32_e32 v196, v197, v195
	v_med3_i32 v197, v197, v198, v195
	v_med3_i32 v194, v198, v194, v195
	v_and_or_b32 v195, v157, s26, 9
	v_max_i32_e32 v198, v196, v195
	v_med3_i32 v196, v196, v197, v195
	v_med3_i32 v194, v197, v194, v195
	v_and_or_b32 v195, v158, s26, 10
	v_max_i32_e32 v197, v198, v195
	v_med3_i32 v198, v198, v196, v195
	v_med3_i32 v194, v196, v194, v195
	v_and_or_b32 v195, v159, s26, 11
	v_max_i32_e32 v196, v197, v195
	v_med3_i32 v197, v197, v198, v195
	v_med3_i32 v194, v198, v194, v195
	v_and_or_b32 v195, v152, s26, 12
	v_max_i32_e32 v198, v196, v195
	v_med3_i32 v196, v196, v197, v195
	v_med3_i32 v194, v197, v194, v195
	v_and_or_b32 v195, v153, s26, 13
	v_max_i32_e32 v197, v198, v195
	v_med3_i32 v198, v198, v196, v195
	v_med3_i32 v194, v196, v194, v195
	v_and_or_b32 v195, v154, s26, 14
	v_max_i32_e32 v196, v197, v195
	v_med3_i32 v197, v197, v198, v195
	v_med3_i32 v194, v198, v194, v195
	v_and_or_b32 v195, v155, s26, 15
	v_max_i32_e32 v198, v196, v195
	v_med3_i32 v196, v196, v197, v195
	v_med3_i32 v194, v197, v194, v195
	v_and_or_b32 v195, v144, s26, 16
	v_max_i32_e32 v197, v198, v195
	v_med3_i32 v198, v198, v196, v195
	v_med3_i32 v194, v196, v194, v195
	v_and_or_b32 v195, v145, s26, 17
	v_max_i32_e32 v196, v197, v195
	v_med3_i32 v197, v197, v198, v195
	v_med3_i32 v194, v198, v194, v195
	v_and_or_b32 v195, v146, s26, 18
	v_max_i32_e32 v198, v196, v195
	v_med3_i32 v196, v196, v197, v195
	v_med3_i32 v194, v197, v194, v195
	v_and_or_b32 v195, v147, s26, 19
	v_max_i32_e32 v197, v198, v195
	v_med3_i32 v198, v198, v196, v195
	v_med3_i32 v194, v196, v194, v195
	v_and_or_b32 v195, v136, s26, 20
	v_max_i32_e32 v196, v197, v195
	v_med3_i32 v197, v197, v198, v195
	v_med3_i32 v194, v198, v194, v195
	v_and_or_b32 v195, v137, s26, 21
	v_max_i32_e32 v198, v196, v195
	v_med3_i32 v196, v196, v197, v195
	v_med3_i32 v194, v197, v194, v195
	v_and_or_b32 v195, v138, s26, 22
	v_max_i32_e32 v197, v198, v195
	v_med3_i32 v198, v198, v196, v195
	v_med3_i32 v194, v196, v194, v195
	v_and_or_b32 v195, v139, s26, 23
	v_max_i32_e32 v196, v197, v195
	v_med3_i32 v197, v197, v198, v195
	v_med3_i32 v194, v198, v194, v195
	v_and_or_b32 v195, v128, s26, 24
	v_max_i32_e32 v198, v196, v195
	v_med3_i32 v196, v196, v197, v195
	v_med3_i32 v194, v197, v194, v195
	v_and_or_b32 v195, v129, s26, 25
	v_max_i32_e32 v197, v198, v195
	v_med3_i32 v198, v198, v196, v195
	v_med3_i32 v194, v196, v194, v195
	v_and_or_b32 v195, v130, s26, 26
	v_max_i32_e32 v196, v197, v195
	v_med3_i32 v197, v197, v198, v195
	v_med3_i32 v194, v198, v194, v195
	v_and_or_b32 v195, v131, s26, 27
	v_max_i32_e32 v198, v196, v195
	v_med3_i32 v196, v196, v197, v195
	v_med3_i32 v194, v197, v194, v195
	v_and_or_b32 v195, v120, s26, 28
	v_max_i32_e32 v197, v198, v195
	v_med3_i32 v198, v198, v196, v195
	v_med3_i32 v194, v196, v194, v195
	v_and_or_b32 v195, v121, s26, 29
	v_mov_b32_e32 v188, v0
	v_max_i32_e32 v196, v197, v195
	v_med3_i32 v197, v197, v198, v195
	v_med3_i32 v194, v198, v194, v195
	v_and_or_b32 v195, v122, s26, 30
	v_max_i32_e32 v198, v196, v195
	v_bfe_u32 v190, v188, 4, 2
	v_med3_i32 v196, v196, v197, v195
	v_med3_i32 v194, v197, v194, v195
	v_and_or_b32 v195, v123, s26, 31
	v_lshlrev_b32_e32 v193, 5, v190
	v_med3_i32 v194, v196, v194, v195
	v_max_i32_e32 v197, v198, v195
	v_med3_i32 v198, v198, v196, v195
	v_or_b32_e32 v214, v194, v193
	v_and_b32_e32 v194, 0xffffff80, v148
	v_and_or_b32 v195, v149, s26, 1
	v_or_b32_e32 v212, v197, v193
	v_or_b32_e32 v213, v198, v193
	v_max_i32_e32 v196, v194, v195
	v_min_i32_e32 v197, v194, v195
	v_and_or_b32 v198, v150, s26, 2
	v_max_i32_e32 v196, v196, v198
	v_med3_i32 v194, v194, v195, v198
	v_min_i32_e32 v195, v197, v198
	v_and_or_b32 v197, v151, s26, 3
	v_max_i32_e32 v198, v196, v197
	v_med3_i32 v196, v196, v194, v197
	v_min_i32_e32 v194, v194, v197
	v_max_i32_e32 v194, v195, v194
	v_and_or_b32 v195, v140, s26, 4
	v_max_i32_e32 v197, v198, v195
	v_med3_i32 v198, v198, v196, v195
	v_med3_i32 v194, v196, v194, v195
	v_and_or_b32 v195, v141, s26, 5
	v_max_i32_e32 v196, v197, v195
	v_med3_i32 v197, v197, v198, v195
	v_med3_i32 v194, v198, v194, v195
	v_and_or_b32 v195, v142, s26, 6
	v_max_i32_e32 v198, v196, v195
	v_med3_i32 v196, v196, v197, v195
	v_med3_i32 v194, v197, v194, v195
	v_and_or_b32 v195, v143, s26, 7
	v_max_i32_e32 v197, v198, v195
	v_med3_i32 v198, v198, v196, v195
	v_med3_i32 v194, v196, v194, v195
	v_and_or_b32 v195, v132, s26, 8
	v_max_i32_e32 v196, v197, v195
	v_med3_i32 v197, v197, v198, v195
	v_med3_i32 v194, v198, v194, v195
	v_and_or_b32 v195, v133, s26, 9
	v_max_i32_e32 v198, v196, v195
	v_med3_i32 v196, v196, v197, v195
	v_med3_i32 v194, v197, v194, v195
	v_and_or_b32 v195, v134, s26, 10
	v_max_i32_e32 v197, v198, v195
	v_med3_i32 v198, v198, v196, v195
	v_med3_i32 v194, v196, v194, v195
	v_and_or_b32 v195, v135, s26, 11
	v_max_i32_e32 v196, v197, v195
	v_med3_i32 v197, v197, v198, v195
	v_med3_i32 v194, v198, v194, v195
	v_and_or_b32 v195, v124, s26, 12
	v_max_i32_e32 v198, v196, v195
	v_med3_i32 v196, v196, v197, v195
	v_med3_i32 v194, v197, v194, v195
	v_and_or_b32 v195, v125, s26, 13
	v_max_i32_e32 v197, v198, v195
	v_med3_i32 v198, v198, v196, v195
	v_med3_i32 v194, v196, v194, v195
	v_and_or_b32 v195, v126, s26, 14
	v_max_i32_e32 v196, v197, v195
	v_med3_i32 v197, v197, v198, v195
	v_med3_i32 v194, v198, v194, v195
	v_and_or_b32 v195, v127, s26, 15
	v_max_i32_e32 v198, v196, v195
	v_med3_i32 v196, v196, v197, v195
	v_med3_i32 v194, v197, v194, v195
	v_and_or_b32 v195, v116, s26, 16
	v_max_i32_e32 v197, v198, v195
	v_med3_i32 v198, v198, v196, v195
	v_med3_i32 v194, v196, v194, v195
	v_and_or_b32 v195, v117, s26, 17
	v_max_i32_e32 v196, v197, v195
	v_med3_i32 v197, v197, v198, v195
	v_med3_i32 v194, v198, v194, v195
	v_and_or_b32 v195, v118, s26, 18
	v_max_i32_e32 v198, v196, v195
	v_med3_i32 v196, v196, v197, v195
	v_med3_i32 v194, v197, v194, v195
	v_and_or_b32 v195, v119, s26, 19
	v_max_i32_e32 v197, v198, v195
	v_med3_i32 v198, v198, v196, v195
	v_med3_i32 v194, v196, v194, v195
	v_and_or_b32 v195, v108, s26, 20
	v_max_i32_e32 v196, v197, v195
	v_med3_i32 v197, v197, v198, v195
	v_med3_i32 v194, v198, v194, v195
	v_and_or_b32 v195, v109, s26, 21
	v_max_i32_e32 v198, v196, v195
	v_med3_i32 v196, v196, v197, v195
	v_med3_i32 v194, v197, v194, v195
	v_and_or_b32 v195, v110, s26, 22
	v_max_i32_e32 v197, v198, v195
	v_med3_i32 v198, v198, v196, v195
	v_med3_i32 v194, v196, v194, v195
	v_and_or_b32 v195, v111, s26, 23
	v_max_i32_e32 v196, v197, v195
	v_med3_i32 v197, v197, v198, v195
	v_med3_i32 v194, v198, v194, v195
	v_and_or_b32 v195, v104, s26, 24
	v_max_i32_e32 v198, v196, v195
	v_med3_i32 v196, v196, v197, v195
	v_med3_i32 v194, v197, v194, v195
	v_and_or_b32 v195, v105, s26, 25
	v_max_i32_e32 v197, v198, v195
	v_med3_i32 v198, v198, v196, v195
	v_med3_i32 v194, v196, v194, v195
	v_and_or_b32 v195, v106, s26, 26
	v_max_i32_e32 v196, v197, v195
	v_med3_i32 v197, v197, v198, v195
	v_med3_i32 v194, v198, v194, v195
	v_and_or_b32 v195, v107, s26, 27
	v_max_i32_e32 v198, v196, v195
	v_med3_i32 v196, v196, v197, v195
	v_med3_i32 v194, v197, v194, v195
	v_and_or_b32 v195, v96, s26, 28
	v_max_i32_e32 v197, v198, v195
	v_med3_i32 v198, v198, v196, v195
	v_med3_i32 v194, v196, v194, v195
	v_and_or_b32 v195, v97, s26, 29
	v_ashrrev_i32_e32 v189, 6, v188
	v_max_i32_e32 v196, v197, v195
	v_med3_i32 v197, v197, v198, v195
	v_med3_i32 v194, v198, v194, v195
	v_and_or_b32 v195, v98, s26, 30
	v_and_b32_e32 v192, 63, v188
	v_lshl_add_u32 v191, v189, 12, s25
	v_max_i32_e32 v198, v196, v195
	v_med3_i32 v196, v196, v197, v195
	v_med3_i32 v194, v197, v194, v195
	v_and_or_b32 v195, v99, s26, 31
	v_lshl_add_u32 v192, v192, 4, v191
	v_med3_i32 v194, v196, v194, v195
	ds_write_b128 v192, v[212:215]
	v_max_i32_e32 v197, v198, v195
	v_med3_i32 v198, v198, v196, v195
	v_or_b32_e32 v214, v194, v193
	v_and_b32_e32 v194, 0xffffff80, v112
	v_and_or_b32 v195, v113, s26, 1
	v_or_b32_e32 v212, v197, v193
	v_or_b32_e32 v213, v198, v193
	v_max_i32_e32 v196, v194, v195
	v_min_i32_e32 v197, v194, v195
	v_and_or_b32 v198, v114, s26, 2
	v_max_i32_e32 v196, v196, v198
	v_med3_i32 v194, v194, v195, v198
	v_min_i32_e32 v195, v197, v198
	v_and_or_b32 v197, v115, s26, 3
	v_max_i32_e32 v198, v196, v197
	v_med3_i32 v196, v196, v194, v197
	v_min_i32_e32 v194, v194, v197
	v_max_i32_e32 v194, v195, v194
	v_and_or_b32 v195, v100, s26, 4
	v_max_i32_e32 v197, v198, v195
	v_med3_i32 v198, v198, v196, v195
	v_med3_i32 v194, v196, v194, v195
	v_and_or_b32 v195, v101, s26, 5
	v_max_i32_e32 v196, v197, v195
	v_med3_i32 v197, v197, v198, v195
	v_med3_i32 v194, v198, v194, v195
	v_and_or_b32 v195, v102, s26, 6
	v_max_i32_e32 v198, v196, v195
	v_med3_i32 v196, v196, v197, v195
	v_med3_i32 v194, v197, v194, v195
	v_and_or_b32 v195, v103, s26, 7
	v_max_i32_e32 v197, v198, v195
	v_med3_i32 v198, v198, v196, v195
	v_med3_i32 v194, v196, v194, v195
	v_and_or_b32 v195, v92, s26, 8
	v_max_i32_e32 v196, v197, v195
	v_med3_i32 v197, v197, v198, v195
	v_med3_i32 v194, v198, v194, v195
	v_and_or_b32 v195, v93, s26, 9
	v_max_i32_e32 v198, v196, v195
	v_med3_i32 v196, v196, v197, v195
	v_med3_i32 v194, v197, v194, v195
	v_and_or_b32 v195, v94, s26, 10
	v_max_i32_e32 v197, v198, v195
	v_med3_i32 v198, v198, v196, v195
	v_med3_i32 v194, v196, v194, v195
	v_and_or_b32 v195, v95, s26, 11
	v_max_i32_e32 v196, v197, v195
	v_med3_i32 v197, v197, v198, v195
	v_med3_i32 v194, v198, v194, v195
	v_and_or_b32 v195, v88, s26, 12
	v_max_i32_e32 v198, v196, v195
	v_med3_i32 v196, v196, v197, v195
	v_med3_i32 v194, v197, v194, v195
	v_and_or_b32 v195, v89, s26, 13
	v_max_i32_e32 v197, v198, v195
	v_med3_i32 v198, v198, v196, v195
	v_med3_i32 v194, v196, v194, v195
	v_and_or_b32 v195, v90, s26, 14
	v_max_i32_e32 v196, v197, v195
	v_med3_i32 v197, v197, v198, v195
	v_med3_i32 v194, v198, v194, v195
	v_and_or_b32 v195, v91, s26, 15
	v_max_i32_e32 v198, v196, v195
	v_med3_i32 v196, v196, v197, v195
	v_med3_i32 v194, v197, v194, v195
	v_and_or_b32 v195, v80, s26, 16
	v_max_i32_e32 v197, v198, v195
	v_med3_i32 v198, v198, v196, v195
	v_med3_i32 v194, v196, v194, v195
	v_and_or_b32 v195, v81, s26, 17
	v_max_i32_e32 v196, v197, v195
	v_med3_i32 v197, v197, v198, v195
	v_med3_i32 v194, v198, v194, v195
	v_and_or_b32 v195, v82, s26, 18
	v_max_i32_e32 v198, v196, v195
	v_med3_i32 v196, v196, v197, v195
	v_med3_i32 v194, v197, v194, v195
	v_and_or_b32 v195, v83, s26, 19
	v_max_i32_e32 v197, v198, v195
	v_med3_i32 v198, v198, v196, v195
	v_med3_i32 v194, v196, v194, v195
	v_and_or_b32 v195, v72, s26, 20
	v_max_i32_e32 v196, v197, v195
	v_med3_i32 v197, v197, v198, v195
	v_med3_i32 v194, v198, v194, v195
	v_and_or_b32 v195, v73, s26, 21
	v_max_i32_e32 v198, v196, v195
	v_med3_i32 v196, v196, v197, v195
	v_med3_i32 v194, v197, v194, v195
	v_and_or_b32 v195, v74, s26, 22
	v_max_i32_e32 v197, v198, v195
	v_med3_i32 v198, v198, v196, v195
	v_med3_i32 v194, v196, v194, v195
	v_and_or_b32 v195, v75, s26, 23
	v_max_i32_e32 v196, v197, v195
	v_med3_i32 v197, v197, v198, v195
	v_med3_i32 v194, v198, v194, v195
	v_and_or_b32 v195, v64, s26, 24
	v_max_i32_e32 v198, v196, v195
	v_med3_i32 v196, v196, v197, v195
	v_med3_i32 v194, v197, v194, v195
	v_and_or_b32 v195, v65, s26, 25
	v_max_i32_e32 v197, v198, v195
	v_med3_i32 v198, v198, v196, v195
	v_med3_i32 v194, v196, v194, v195
	v_and_or_b32 v195, v66, s26, 26
	v_max_i32_e32 v196, v197, v195
	v_med3_i32 v197, v197, v198, v195
	v_med3_i32 v194, v198, v194, v195
	v_and_or_b32 v195, v67, s26, 27
	v_max_i32_e32 v198, v196, v195
	v_med3_i32 v196, v196, v197, v195
	v_med3_i32 v194, v197, v194, v195
	v_and_or_b32 v195, v56, s26, 28
	v_max_i32_e32 v197, v198, v195
	v_med3_i32 v198, v198, v196, v195
	v_med3_i32 v194, v196, v194, v195
	v_and_or_b32 v195, v57, s26, 29
	v_max_i32_e32 v196, v197, v195
	v_med3_i32 v197, v197, v198, v195
	v_med3_i32 v194, v198, v194, v195
	v_and_or_b32 v195, v58, s26, 30
	v_max_i32_e32 v198, v196, v195
	v_med3_i32 v196, v196, v197, v195
	v_med3_i32 v194, v197, v194, v195
	v_and_or_b32 v195, v59, s26, 31
	v_med3_i32 v194, v196, v194, v195
	ds_write_b128 v192, v[212:215] offset:1024
	s_waitcnt vmcnt(0)
	s_barrier
	s_and_b64 vcc, exec, s[10:11]
	s_cbranch_vccnz .Lmid_skip
	s_add_u32 s68, s68, 0x6000
	s_addc_u32 s69, s69, 0
	s_add_u32 s70, s70, 0x6000
	s_addc_u32 s71, s71, 0
	s_mov_b32 m0, s60
	s_nop 0
	global_load_lds_dwordx4 v228, s[68:69]
	s_mov_b32 m0, s61
	s_nop 0
	global_load_lds_dwordx4 v229, s[68:69]
	s_mov_b32 m0, s62
	s_nop 0
	global_load_lds_dwordx4 v230, s[68:69]
	s_mov_b32 m0, s63
	s_nop 0
	global_load_lds_dwordx4 v228, s[70:71]
	s_mov_b32 m0, s64
	s_nop 0
	global_load_lds_dwordx4 v229, s[70:71]
	s_mov_b32 m0, s65
	s_nop 0
	global_load_lds_dwordx4 v230, s[70:71]
	ds_read_b128 v[2:5], v170 offset:12288
	ds_read_b64 v[6:7], v173 offset:12352
	ds_read_b128 v[8:11], v170 offset:13824
	ds_read_b64 v[12:13], v173 offset:13888
	ds_read_b128 v[14:17], v170 offset:15360
	ds_read_b64 v[18:19], v173 offset:15424
	ds_read_b128 v[26:29], v170 offset:16896
	ds_read_b64 v[30:31], v173 offset:16960
	ds_read_b128 v[20:23], v1
	ds_read_b64 v[24:25], v172 offset:64
	ds_read_b128 v[32:35], v1 offset:1536
	ds_read_b64 v[36:37], v172 offset:1600
.Lmid_skip:
	v_max_i32_e32 v197, v198, v195
	v_med3_i32 v198, v198, v196, v195
	v_or_b32_e32 v214, v194, v193
	v_and_b32_e32 v194, 0xffffff80, v84
	v_and_or_b32 v195, v85, s26, 1
	v_or_b32_e32 v212, v197, v193
	v_or_b32_e32 v213, v198, v193
	v_max_i32_e32 v196, v194, v195
	v_min_i32_e32 v197, v194, v195
	v_and_or_b32 v198, v86, s26, 2
	v_max_i32_e32 v196, v196, v198
	v_med3_i32 v194, v194, v195, v198
	v_min_i32_e32 v195, v197, v198
	v_and_or_b32 v197, v87, s26, 3
	v_max_i32_e32 v198, v196, v197
	v_med3_i32 v196, v196, v194, v197
	v_min_i32_e32 v194, v194, v197
	v_max_i32_e32 v194, v195, v194
	v_and_or_b32 v195, v76, s26, 4
	v_max_i32_e32 v197, v198, v195
	v_med3_i32 v198, v198, v196, v195
	v_med3_i32 v194, v196, v194, v195
	v_and_or_b32 v195, v77, s26, 5
	v_max_i32_e32 v196, v197, v195
	v_med3_i32 v197, v197, v198, v195
	v_med3_i32 v194, v198, v194, v195
	v_and_or_b32 v195, v78, s26, 6
	v_max_i32_e32 v198, v196, v195
	v_med3_i32 v196, v196, v197, v195
	v_med3_i32 v194, v197, v194, v195
	v_and_or_b32 v195, v79, s26, 7
	v_max_i32_e32 v197, v198, v195
	v_med3_i32 v198, v198, v196, v195
	v_med3_i32 v194, v196, v194, v195
	v_and_or_b32 v195, v68, s26, 8
	v_max_i32_e32 v196, v197, v195
	v_med3_i32 v197, v197, v198, v195
	v_med3_i32 v194, v198, v194, v195
	v_and_or_b32 v195, v69, s26, 9
	v_max_i32_e32 v198, v196, v195
	v_med3_i32 v196, v196, v197, v195
	v_med3_i32 v194, v197, v194, v195
	v_and_or_b32 v195, v70, s26, 10
	v_max_i32_e32 v197, v198, v195
	v_med3_i32 v198, v198, v196, v195
	v_med3_i32 v194, v196, v194, v195
	v_and_or_b32 v195, v71, s26, 11
	v_max_i32_e32 v196, v197, v195
	v_med3_i32 v197, v197, v198, v195
	v_med3_i32 v194, v198, v194, v195
	v_and_or_b32 v195, v60, s26, 12
	v_max_i32_e32 v198, v196, v195
	v_med3_i32 v196, v196, v197, v195
	v_med3_i32 v194, v197, v194, v195
	v_and_or_b32 v195, v61, s26, 13
	v_max_i32_e32 v197, v198, v195
	v_med3_i32 v198, v198, v196, v195
	v_med3_i32 v194, v196, v194, v195
	v_and_or_b32 v195, v62, s26, 14
	v_max_i32_e32 v196, v197, v195
	v_med3_i32 v197, v197, v198, v195
	v_med3_i32 v194, v198, v194, v195
	v_and_or_b32 v195, v63, s26, 15
	v_max_i32_e32 v198, v196, v195
	v_med3_i32 v196, v196, v197, v195
	v_med3_i32 v194, v197, v194, v195
	v_and_or_b32 v195, v52, s26, 16
	v_max_i32_e32 v197, v198, v195
	v_med3_i32 v198, v198, v196, v195
	v_med3_i32 v194, v196, v194, v195
	v_and_or_b32 v195, v53, s26, 17
	v_max_i32_e32 v196, v197, v195
	v_med3_i32 v197, v197, v198, v195
	v_med3_i32 v194, v198, v194, v195
	v_and_or_b32 v195, v54, s26, 18
	v_max_i32_e32 v198, v196, v195
	v_med3_i32 v196, v196, v197, v195
	v_med3_i32 v194, v197, v194, v195
	v_and_or_b32 v195, v55, s26, 19
	v_max_i32_e32 v197, v198, v195
	v_med3_i32 v198, v198, v196, v195
	v_med3_i32 v194, v196, v194, v195
	v_and_or_b32 v195, v48, s26, 20
	v_max_i32_e32 v196, v197, v195
	v_med3_i32 v197, v197, v198, v195
	v_med3_i32 v194, v198, v194, v195
	v_and_or_b32 v195, v49, s26, 21
	v_max_i32_e32 v198, v196, v195
	v_med3_i32 v196, v196, v197, v195
	v_med3_i32 v194, v197, v194, v195
	v_and_or_b32 v195, v50, s26, 22
	v_max_i32_e32 v197, v198, v195
	v_med3_i32 v198, v198, v196, v195
	v_med3_i32 v194, v196, v194, v195
	v_and_or_b32 v195, v51, s26, 23
	v_max_i32_e32 v196, v197, v195
	v_med3_i32 v197, v197, v198, v195
	v_med3_i32 v194, v198, v194, v195
	v_and_or_b32 v195, v44, s26, 24
	v_max_i32_e32 v198, v196, v195
	v_med3_i32 v196, v196, v197, v195
	v_med3_i32 v194, v197, v194, v195
	v_and_or_b32 v195, v45, s26, 25
	v_max_i32_e32 v197, v198, v195
	v_med3_i32 v198, v198, v196, v195
	v_med3_i32 v194, v196, v194, v195
	v_and_or_b32 v195, v46, s26, 26
	v_max_i32_e32 v196, v197, v195
	v_med3_i32 v197, v197, v198, v195
	v_med3_i32 v194, v198, v194, v195
	v_and_or_b32 v195, v47, s26, 27
	v_max_i32_e32 v198, v196, v195
	v_med3_i32 v196, v196, v197, v195
	v_med3_i32 v194, v197, v194, v195
	v_and_or_b32 v195, v40, s26, 28
	v_max_i32_e32 v197, v198, v195
	v_med3_i32 v198, v198, v196, v195
	v_med3_i32 v194, v196, v194, v195
	v_and_or_b32 v195, v41, s26, 29
	v_max_i32_e32 v196, v197, v195
	v_med3_i32 v197, v197, v198, v195
	v_med3_i32 v194, v198, v194, v195
	v_and_or_b32 v195, v42, s26, 30
	v_max_i32_e32 v198, v196, v195
	v_med3_i32 v196, v196, v197, v195
	v_med3_i32 v194, v197, v194, v195
	v_and_or_b32 v195, v43, s26, 31
	v_max_i32_e32 v197, v198, v195
	v_med3_i32 v198, v198, v196, v195
	v_med3_i32 v194, v196, v194, v195
	ds_write_b128 v192, v[212:215] offset:2048
	v_or_b32_e32 v212, v197, v193
	v_or_b32_e32 v213, v198, v193
	v_or_b32_e32 v214, v194, v193
	v_and_b32_e32 v209, 15, v188
	ds_write_b128 v192, v[212:215] offset:3072
	v_lshlrev_b32_e32 v190, 10, v190
	v_lshlrev_b32_e32 v192, 4, v209
	s_waitcnt lgkmcnt(0)
	v_add3_u32 v202, v191, v190, v192
	ds_read_b128 v[190:193], v202
	ds_read_b128 v[194:197], v202 offset:256
	ds_read_b128 v[198:201], v202 offset:512
	ds_read_b128 v[202:205], v202 offset:768
	v_lshlrev_b32_e32 v189, 5, v189
	s_lshl_b32 s34, s34, 8
	v_ashrrev_i32_e32 v210, 8, v188
	s_waitcnt lgkmcnt(0)
	v_max_i32_e32 v193, v190, v191
	v_min_i32_e32 v197, v190, v191
	v_max_i32_e32 v193, v193, v192
	v_med3_i32 v190, v190, v191, v192
	v_min_i32_e32 v191, v197, v192
	v_max_i32_e32 v197, v193, v194
	v_med3_i32 v193, v193, v190, v194
	v_min_i32_e32 v190, v190, v194
	v_max_i32_e32 v190, v191, v190
	v_min_i32_e32 v191, v191, v194
	v_max_i32_e32 v194, v197, v195
	v_med3_i32 v197, v197, v193, v195
	v_med3_i32 v193, v193, v190, v195
	v_min_i32_e32 v190, v190, v195
	v_max_i32_e32 v190, v191, v190
	v_max_i32_e32 v191, v194, v196
	v_med3_i32 v194, v194, v197, v196
	v_med3_i32 v195, v197, v193, v196
	v_med3_i32 v190, v193, v190, v196
	v_max_i32_e32 v193, v191, v198
	v_med3_i32 v191, v191, v194, v198
	v_med3_i32 v194, v194, v195, v198
	v_med3_i32 v190, v195, v190, v198
	v_max_i32_e32 v195, v193, v199
	v_med3_i32 v193, v193, v191, v199
	v_med3_i32 v191, v191, v194, v199
	v_med3_i32 v190, v194, v190, v199
	v_max_i32_e32 v194, v195, v200
	v_med3_i32 v195, v195, v193, v200
	v_med3_i32 v193, v193, v191, v200
	v_med3_i32 v190, v191, v190, v200
	v_max_i32_e32 v191, v194, v202
	v_med3_i32 v194, v194, v195, v202
	v_med3_i32 v195, v195, v193, v202
	v_med3_i32 v190, v193, v190, v202
	v_max_i32_e32 v193, v191, v203
	v_med3_i32 v191, v191, v194, v203
	v_max_i32_e32 v206, v193, v204
	v_med3_i32 v207, v193, v191, v204
	v_max_i32_e32 v193, v200, v204
	v_max3_i32 v192, v192, v196, v193
	v_lshlrev_b32_e32 v193, 2, v188
	v_and_b32_e32 v189, 0x60, v189
	v_and_b32_e32 v188, 16, v188
	s_lshl_b32 s36, s13, 1
	v_med3_i32 v194, v194, v195, v203
	v_med3_i32 v190, v195, v190, v203
	v_and_b32_e32 v193, 0x80, v193
	v_or3_b32 v188, v188, s34, v189
	s_ashr_i32 s37, s36, 31
	v_ashrrev_i32_e32 v211, 31, v210
	v_med3_i32 v208, v191, v194, v204
	v_min_i32_e32 v191, v194, v190
	v_max_i32_e32 v190, v194, v190
	v_or3_b32 v193, v188, v193, v209
	v_lshl_add_u64 v[188:189], v[210:211], 0, s[36:37]
	v_min_i32_e32 v190, v190, v204
	v_mad_i64_i32 v[188:189], s[36:37], v193, s27, v[188:189]
	v_max3_i32 v209, v191, v190, v192
	v_lshl_add_u64 v[188:189], v[188:189], 4, s[8:9]
	s_andn2_b64 vcc, exec, s[10:11]
	s_mov_b32 s13, s3
	s_mov_b32 s34, s35
	global_store_dwordx4 v[188:189], v[206:209], off
	s_cbranch_vccz .LBB1_8
.LBB1_2:
	s_mul_i32 s41, s34, 0x30000
	s_mul_hi_i32 s40, s34, 0x30000
	s_add_u32 s11, s6, s41
	s_addc_u32 s35, s7, s40
	s_mov_b32 s10, s2
	s_add_u32 s2, s11, 0x6000
	s_addc_u32 s3, s35, 0
	s_mul_i32 s43, s13, 0x30000
	s_mul_hi_i32 s42, s13, 0x30000
	s_add_u32 s44, s4, s43
	s_addc_u32 s45, s5, s42
	s_add_u32 s38, s11, 0x8000
	s_addc_u32 s39, s35, 0
	s_add_u32 s46, s44, 0x5000
	s_addc_u32 s47, s45, 0
	s_and_b64 s[36:37], s[0:1], exec
	s_cselect_b32 s37, s39, s47
	s_cselect_b32 s36, s38, s46
	s_add_u32 s38, s44, 0x7000
	s_addc_u32 s39, s45, 0
	s_add_u32 s2, s11, 0x9000
	s_addc_u32 s3, s35, 0
	s_add_u32 s11, s11, 0xb000
	s_addc_u32 s35, s35, 0
	s_add_u32 s38, s44, 0x8000
	s_addc_u32 s39, s45, 0
	s_and_b64 s[36:37], s[0:1], exec
	s_cselect_b32 s37, s35, s39
	s_cselect_b32 s36, s11, s38
	s_add_u32 s38, s44, 0xa000
	s_addc_u32 s39, s45, 0
	s_add_u32 s11, s21, s43
	s_addc_u32 s35, s22, s42
	s_add_u32 s2, s23, s41
	s_addc_u32 s3, s24, s40
	s_mov_b32 s36, -2
	s_waitcnt lgkmcnt(0)
